# lazy-rescale threshold 16 (rescale essentially only in the first key sub-block); three scalar add pairs of the row sums packed
# baseline (speedup 1.0000x reference)
;     ...
;                 mx = fmaxf(mx, __shfl_xor(mx, 32));
;                 const float mnew = fmaxf(mrun, mx); const bool grew = __any(mnew > mrun);
;                 if (grew) {
;                     const float alpha = __builtin_amdgcn_exp2f((mrun - mnew) * L2E);
;                     ls0 *= alpha; ls1 *= alpha; ls2 *= alpha; ls3 *= alpha;
; #pragma unroll
;                     for (int i = 0; i < 16; ++i) { oacc[0][i] *= alpha; oacc[1][i] *= alpha; } }
;                 mrun = mnew;
.LBB0_2233:
	v_mov_b32_e32 v32, v64
	s_nop 1
	v_permlane32_swap_b32_e32 v32, v64
	v_max3_f32 v32, v202, v64, v32
	s_cmp_eq_u32 s21, 0
	s_cbranch_scc1 .LBB0_2235
	v_add_f32_e32 v33, 0x41800000, v202
	v_cmp_gt_f32_e32 vcc, v32, v33
	s_cbranch_vccnz .Lattn_resc
	v_mov_b32_e32 v32, v202
	s_branch .LBB0_2235

; #define LAS __attribute__((address_space(3)))
; DI unsigned pk2(float lo, float hi) { f32x2 v = {lo, hi}; return __builtin_bit_cast(unsigned, __builtin_convertvector(v, bf16v2)); }
;     ...
;                     for (int i = 0; i < 16; i += 4) { const float p0 = __builtin_amdgcn_exp2f(__builtin_fmaf(sacc[k2][i], L2E, nm)), p1 = __builtin_amdgcn_exp2f(__builtin_fmaf(sacc[k2][i + 1], L2E, nm)),
;                                                                   p2 = __builtin_amdgcn_exp2f(__builtin_fmaf(sacc[k2][i + 2], L2E, nm)), p3 = __builtin_amdgcn_exp2f(__builtin_fmaf(sacc[k2][i + 3], L2E, nm));
;                         sacc[k2][i] = p0; sacc[k2][i + 1] = p1; sacc[k2][i + 2] = p2; sacc[k2][i + 3] = p3; ls0 += p0; ls1 += p1; ls2 += p2; ls3 += p3; }
; #pragma unroll
;                     for (int cc = 0; cc < 2; ++cc) {
;                         u32x4 pw; pw.x = pk2(sacc[k2][8 * cc], sacc[k2][8 * cc + 1]); pw.y = pk2(sacc[k2][8 * cc + 2], sacc[k2][8 * cc + 3]); pw.z = pk2(sacc[k2][8 * cc + 4], sacc[k2][8 * cc + 5]); pw.w = pk2(sacc[k2][8 * cc + 6], sacc[k2][8 * cc + 7]);
;                         const bf16x8 pf = __builtin_bit_cast(bf16x8, pw);
;                         const int key0 = 32 * kt + 16 * cc + 4 * half;
; #pragma unroll
;                         for (int dt = 0; dt < 2; ++dt) { const LAS unsigned char* vb = Vt + (32 * dt + qi) * VT_PITCH + key0 * 2;
;                             const u32x2 va = *(const LAS u32x2*)vb, vb2 = *(const LAS u32x2*)(vb + 16);
;                             u32x4 vw; vw.x = va.x; vw.y = va.y; vw.z = vb2.x; vw.w = vb2.y;
;                             oacc[dt] = __builtin_amdgcn_mfma_f32_32x32x16_bf16(__builtin_bit_cast(bf16x8, vw), pf, oacc[dt], 0, 0, 0); } } }
.LBB0_2235:
	v_mul_f32_e32 v33, 0xbfb8aa3b, v32
	v_pk_fma_f32 v[126:127], v[126:127], v[228:229], v[32:33] op_sel:[0,0,1] op_sel_hi:[1,0,1]
	v_pk_fma_f32 v[122:123], v[122:123], v[228:229], v[32:33] op_sel:[0,0,1] op_sel_hi:[1,0,1]
	v_exp_f32_e32 v63, v126
	v_pk_fma_f32 v[128:129], v[128:129], v[228:229], v[32:33] op_sel:[0,0,1] op_sel_hi:[1,0,1]
	v_exp_f32_e32 v62, v127
	v_pk_fma_f32 v[124:125], v[124:125], v[228:229], v[32:33] op_sel:[0,0,1] op_sel_hi:[1,0,1]
	v_exp_f32_e32 v61, v122
	v_exp_f32_e32 v60, v123
	v_exp_f32_e32 v123, v128
	v_exp_f32_e32 v122, v129
	v_pk_fma_f32 v[130:131], v[130:131], v[228:229], v[32:33] op_sel:[0,0,1] op_sel_hi:[1,0,1]
	v_exp_f32_e32 v35, v124
	v_exp_f32_e32 v34, v125
	v_exp_f32_e32 v125, v130
	v_exp_f32_e32 v124, v131
	v_pk_fma_f32 v[132:133], v[132:133], v[228:229], v[32:33] op_sel:[0,0,1] op_sel_hi:[1,0,1]
	v_pk_fma_f32 v[164:165], v[164:165], v[228:229], v[32:33] op_sel:[0,0,1] op_sel_hi:[1,0,1]
	v_exp_f32_e32 v127, v132
	v_exp_f32_e32 v126, v133
	v_exp_f32_e32 v133, v164
	v_exp_f32_e32 v132, v165
	v_pk_fma_f32 v[134:135], v[134:135], v[228:229], v[32:33] op_sel:[0,0,1] op_sel_hi:[1,0,1]
	v_pk_fma_f32 v[166:167], v[166:167], v[228:229], v[32:33] op_sel:[0,0,1] op_sel_hi:[1,0,1]
	v_exp_f32_e32 v129, v134
	v_exp_f32_e32 v128, v135
	v_exp_f32_e32 v135, v166
	v_exp_f32_e32 v134, v167
	v_pk_fma_f32 v[136:137], v[136:137], v[228:229], v[32:33] op_sel:[0,0,1] op_sel_hi:[1,0,1]
	v_pk_fma_f32 v[168:169], v[168:169], v[228:229], v[32:33] op_sel:[0,0,1] op_sel_hi:[1,0,1]
	v_exp_f32_e32 v131, v136
	v_exp_f32_e32 v130, v137
	v_exp_f32_e32 v137, v168
	v_exp_f32_e32 v136, v169
	v_pk_fma_f32 v[170:171], v[170:171], v[228:229], v[32:33] op_sel:[0,0,1] op_sel_hi:[1,0,1]
	v_pk_fma_f32 v[172:173], v[172:173], v[228:229], v[32:33] op_sel:[0,0,1] op_sel_hi:[1,0,1]
	v_exp_f32_e32 v165, v170
	v_exp_f32_e32 v164, v171
	v_add_u32_e32 v58, 0x4000, v216
	v_exp_f32_e32 v167, v172
	v_exp_f32_e32 v166, v173
	v_pk_fma_f32 v[174:175], v[174:175], v[228:229], v[32:33] op_sel:[0,0,1] op_sel_hi:[1,0,1]
	ds_read2_b64 v[36:39], v216 offset1:2
	ds_read2_b64 v[40:43], v216 offset0:4 offset1:6
	ds_read2_b64 v[44:47], v58 offset0:32 offset1:34
	ds_read2_b64 v[48:51], v58 offset0:36 offset1:38
	v_pk_fma_f32 v[138:139], v[138:139], v[228:229], v[32:33] op_sel:[0,0,1] op_sel_hi:[1,0,1]
	v_exp_f32_e32 v169, v174
	v_exp_f32_e32 v168, v175
	v_cvt_pk_bf16_f32 v52, v61, v60
	v_cvt_pk_bf16_f32 v53, v35, v34
	v_cvt_pk_bf16_f32 v54, v63, v62
	v_cvt_pk_bf16_f32 v55, v123, v122
	v_exp_f32_e32 v171, v138
	v_exp_f32_e32 v170, v139
	s_waitcnt lgkmcnt(3)
	v_mfma_f32_32x32x16_bf16 v[16:31], v[36:39], v[52:55], v[16:31]
	v_pk_fma_f32 v[140:141], v[140:141], v[228:229], v[32:33] op_sel:[0,0,1] op_sel_hi:[1,0,1]
	v_cvt_pk_bf16_f32 v36, v125, v124
	v_exp_f32_e32 v139, v140
	s_waitcnt lgkmcnt(1)
	v_mfma_f32_32x32x16_bf16 v[0:15], v[44:47], v[52:55], v[0:15]
	v_cvt_pk_bf16_f32 v38, v129, v128
	v_cvt_pk_bf16_f32 v37, v127, v126
	v_pk_add_f32 v[60:61], v[60:61], v[120:121]
	v_cvt_pk_bf16_f32 v39, v131, v130
	v_exp_f32_e32 v138, v141
	s_nop 0
	v_mfma_f32_32x32x16_bf16 v[16:31], v[40:43], v[36:39], v[16:31]
	ds_read2_b64 v[40:43], v216 offset0:8 offset1:10
	ds_read2_b64 v[44:47], v58 offset0:40 offset1:42
	ds_read2_b64 v[52:55], v216 offset0:12 offset1:14
	ds_read2_b64 v[56:59], v58 offset0:44 offset1:46
	v_pk_add_f32 v[34:35], v[34:35], v[118:119]
	v_pk_add_f32 v[34:35], v[122:123], v[34:35]
	s_sub_i32 s21, s21, 64
	v_pk_add_f32 v[34:35], v[126:127], v[34:35]
	s_add_i32 s22, s22, 64
	s_waitcnt lgkmcnt(4)
	v_mfma_f32_32x32x16_bf16 v[0:15], v[48:51], v[36:39], v[0:15]
	v_cvt_pk_bf16_f32 v37, v135, v134
	v_cvt_pk_bf16_f32 v36, v133, v132
	v_cvt_pk_bf16_f32 v38, v137, v136
	v_cvt_pk_bf16_f32 v39, v165, v164
	v_pk_add_f32 v[34:35], v[130:131], v[34:35]
	s_cmpk_eq_i32 s21, 0xff00
	s_waitcnt lgkmcnt(3)
	v_mfma_f32_32x32x16_bf16 v[16:31], v[40:43], v[36:39], v[16:31]
	v_pk_add_f32 v[40:41], v[62:63], v[60:61]
	v_pk_add_f32 v[40:41], v[124:125], v[40:41]
	v_pk_add_f32 v[34:35], v[134:135], v[34:35]
	v_pk_add_f32 v[40:41], v[128:129], v[40:41]
	v_pk_add_f32 v[34:35], v[164:165], v[34:35]
	v_pk_add_f32 v[40:41], v[132:133], v[40:41]
	s_waitcnt lgkmcnt(2)
	v_mfma_f32_32x32x16_bf16 v[0:15], v[44:47], v[36:39], v[0:15]
	v_cvt_pk_bf16_f32 v36, v167, v166
	v_pk_add_f32 v[40:41], v[136:137], v[40:41]
	v_cvt_pk_bf16_f32 v37, v169, v168
	v_pk_add_f32 v[40:41], v[166:167], v[40:41]
	v_cvt_pk_bf16_f32 v38, v171, v170
	v_cvt_pk_bf16_f32 v39, v139, v138
	v_pk_add_f32 v[34:35], v[168:169], v[34:35]
	v_pk_add_f32 v[120:121], v[170:171], v[40:41]
	s_waitcnt lgkmcnt(1)
	v_mfma_f32_32x32x16_bf16 v[16:31], v[52:55], v[36:39], v[16:31]
	v_pk_add_f32 v[118:119], v[138:139], v[34:35]
	v_add_u32_e32 v216, 0x80, v216
	v_add_u32_e32 v251, 0x2400, v251
	s_cselect_b64 s[6:7], -1, 0
	s_waitcnt lgkmcnt(0)
	v_mfma_f32_32x32x16_bf16 v[0:15], v[56:59], v[36:39], v[0:15]
	s_and_b64 vcc, exec, s[6:7]
	s_cbranch_vccnz .LBB0_2238
